# v9 + grid barrier: non-leader WGs poll the top-level generation word directly (one hop less per barrier)
# baseline (speedup 1.0000x reference)
; __device__ __forceinline__ unsigned xb_ld(unsigned* p)              { return __hip_atomic_load(p, __ATOMIC_RELAXED, __HIP_MEMORY_SCOPE_AGENT); }
; __device__ __forceinline__ unsigned xb_add(unsigned* p, unsigned v) { return __hip_atomic_fetch_add(p, v, __ATOMIC_RELAXED, __HIP_MEMORY_SCOPE_AGENT); }
; #define XB_SPIN(cond, bar) do { unsigned _sp = 0; while (cond) { __builtin_amdgcn_s_sleep(1); \
;     if ((++_sp & 255u) == 0u) { if (xb_ld(&(bar)[XB_TMO])) break; if (_sp > XB_SPIN_CAP) { atomicAdd(&(bar)[XB_TMO], 1u); break; } } } } while (0)
; __device__ __forceinline__ void xcd_barrier(const XcdBarrier& b) {
;     ...
;         if (nloc == 0u) { xcd_barrier_complete(bar, b.x, nloc, nx); b.st[0] = nloc; b.st[1] = nx; }
;         const unsigned old = xb_add(&bar[XB_XSUB(b.x)], 1u);
;         const unsigned gen = old / nloc;
;         if (old + 1u == (gen + 1u) * nloc) {
;             __builtin_amdgcn_fence(__ATOMIC_RELEASE, "agent");
;             asm volatile("s_waitcnt vmcnt(0)" ::: "memory");
;             const unsigned og = xb_add(&bar[XB_TOP], 1u);
;             const unsigned tg = og / nx;
;             if (og + 1u == (tg + 1u) * nx) xb_add(&bar[XB_TOPGEN], 1u);
;             else XB_SPIN(xb_ld(&bar[XB_TOPGEN]) == tg, bar);
;             __builtin_amdgcn_fence(__ATOMIC_ACQUIRE, "agent");
;             xb_add(&bar[XB_XGEN(b.x)], 1u);
;             asm volatile("s_waitcnt vmcnt(0)" ::: "memory");
;         } else {
;             XB_SPIN(xb_ld(&bar[XB_XGEN(b.x)]) == gen, bar);
.LBB0_170:
	s_or_b64 exec, exec, s[10:11]
	v_cvt_f32_u32_e32 v5, v3
	s_waitcnt vmcnt(0)
	v_readfirstlane_b32 s2, v4
	s_add_u32 s6, s6, 0x2400
	s_addc_u32 s7, s7, 0
	s_add_u32 s98, s50, 0x7500
	s_addc_u32 s99, s51, 0
	v_rcp_iflag_f32_e32 v5, v5
	v_add_u32_e32 v6, s2, v2
	v_mul_f32_e32 v4, 0x4f7ffffe, v5
	v_cvt_u32_f32_e32 v4, v4
	v_sub_u32_e32 v5, 0, v3
	v_mul_lo_u32 v2, v5, v4
	v_mul_hi_u32 v2, v4, v2
	v_add_u32_e32 v2, v4, v2
	v_mul_hi_u32 v2, v6, v2
	v_mul_lo_u32 v4, v2, v3
	v_sub_u32_e32 v4, v6, v4
	v_add_u32_e32 v5, 1, v2
	v_cmp_ge_u32_e32 vcc, v4, v3
	s_nop 1
	v_cndmask_b32_e32 v2, v2, v5, vcc
	v_sub_u32_e32 v5, v4, v3
	v_cndmask_b32_e32 v4, v4, v5, vcc
	v_add_u32_e32 v5, 1, v2
	v_cmp_ge_u32_e32 vcc, v4, v3
	v_add_u32_e32 v4, 1, v6
	s_nop 0
	v_cndmask_b32_e32 v2, v2, v5, vcc
	v_mul_lo_u32 v5, v3, v2
	v_add_u32_e32 v3, v5, v3
	v_cmp_ne_u32_e32 vcc, v4, v3
	s_and_saveexec_b64 s[2:3], vcc
	s_xor_b64 s[8:9], exec, s[2:3]
	s_cbranch_execz .LBB0_203
	s_waitcnt lgkmcnt(0)
	v_mov_b32_e32 v1, 0
	global_load_dword v3, v1, s[98:99] sc1
	s_waitcnt vmcnt(0)
	v_cmp_eq_u32_e32 vcc, v3, v2
	s_and_saveexec_b64 s[10:11], vcc
	s_cbranch_execz .LBB0_202
	s_mov_b32 s2, 1
	s_mov_b64 s[12:13], 0
	s_branch .LBB0_174

; __device__ __forceinline__ unsigned xb_ld(unsigned* p)              { return __hip_atomic_load(p, __ATOMIC_RELAXED, __HIP_MEMORY_SCOPE_AGENT); }
; #define XB_SPIN(cond, bar) do { unsigned _sp = 0; while (cond) { __builtin_amdgcn_s_sleep(1); \
;     if ((++_sp & 255u) == 0u) { if (xb_ld(&(bar)[XB_TMO])) break; if (_sp > XB_SPIN_CAP) { atomicAdd(&(bar)[XB_TMO], 1u); break; } } } } while (0)
; __device__ __forceinline__ void xcd_barrier(const XcdBarrier& b) {
;     ...
;             XB_SPIN(xb_ld(&bar[XB_XGEN(b.x)]) == gen, bar);
.LBB0_176:
	global_load_dword v3, v1, s[98:99] sc1
	s_add_i32 s2, s2, 1
	s_mov_b64 s[18:19], -1
	s_waitcnt vmcnt(0)
	v_cmp_ne_u32_e32 vcc, v3, v2
	s_orn2_b64 s[16:17], vcc, exec
	s_branch .LBB0_173

; __device__ __forceinline__ unsigned xb_ld(unsigned* p)              { return __hip_atomic_load(p, __ATOMIC_RELAXED, __HIP_MEMORY_SCOPE_AGENT); }
; __device__ __forceinline__ unsigned xb_add(unsigned* p, unsigned v) { return __hip_atomic_fetch_add(p, v, __ATOMIC_RELAXED, __HIP_MEMORY_SCOPE_AGENT); }
; #define XB_SPIN(cond, bar) do { unsigned _sp = 0; while (cond) { __builtin_amdgcn_s_sleep(1); \
;     if ((++_sp & 255u) == 0u) { if (xb_ld(&(bar)[XB_TMO])) break; if (_sp > XB_SPIN_CAP) { atomicAdd(&(bar)[XB_TMO], 1u); break; } } } } while (0)
; __device__ __forceinline__ void xcd_barrier(const XcdBarrier& b) {
;     ...
;         if (nloc == 0u) { xcd_barrier_complete(bar, b.x, nloc, nx); b.st[0] = nloc; b.st[1] = nx; }
;         const unsigned old = xb_add(&bar[XB_XSUB(b.x)], 1u);
;         const unsigned gen = old / nloc;
;         if (old + 1u == (gen + 1u) * nloc) {
;             __builtin_amdgcn_fence(__ATOMIC_RELEASE, "agent");
;             asm volatile("s_waitcnt vmcnt(0)" ::: "memory");
;             const unsigned og = xb_add(&bar[XB_TOP], 1u);
;             const unsigned tg = og / nx;
;             if (og + 1u == (tg + 1u) * nx) xb_add(&bar[XB_TOPGEN], 1u);
;             else XB_SPIN(xb_ld(&bar[XB_TOPGEN]) == tg, bar);
;             __builtin_amdgcn_fence(__ATOMIC_ACQUIRE, "agent");
;             xb_add(&bar[XB_XGEN(b.x)], 1u);
;             asm volatile("s_waitcnt vmcnt(0)" ::: "memory");
;         } else {
;             XB_SPIN(xb_ld(&bar[XB_XGEN(b.x)]) == gen, bar);
.LBB0_255:
	s_or_b64 exec, exec, s[12:13]
	v_cvt_f32_u32_e32 v5, v3
	s_waitcnt vmcnt(0)
	v_readfirstlane_b32 s2, v4
	s_add_u32 s8, s8, 0x2400
	s_addc_u32 s9, s9, 0
	s_add_u32 s98, s50, 0x7500
	s_addc_u32 s99, s51, 0
	v_rcp_iflag_f32_e32 v5, v5
	v_add_u32_e32 v6, s2, v2
	v_mul_f32_e32 v4, 0x4f7ffffe, v5
	v_cvt_u32_f32_e32 v4, v4
	v_sub_u32_e32 v5, 0, v3
	v_mul_lo_u32 v2, v5, v4
	v_mul_hi_u32 v2, v4, v2
	v_add_u32_e32 v2, v4, v2
	v_mul_hi_u32 v2, v6, v2
	v_mul_lo_u32 v4, v2, v3
	v_sub_u32_e32 v4, v6, v4
	v_add_u32_e32 v5, 1, v2
	v_cmp_ge_u32_e32 vcc, v4, v3
	s_nop 1
	v_cndmask_b32_e32 v2, v2, v5, vcc
	v_sub_u32_e32 v5, v4, v3
	v_cndmask_b32_e32 v4, v4, v5, vcc
	v_add_u32_e32 v5, 1, v2
	v_cmp_ge_u32_e32 vcc, v4, v3
	v_add_u32_e32 v4, 1, v6
	s_nop 0
	v_cndmask_b32_e32 v2, v2, v5, vcc
	v_mul_lo_u32 v5, v3, v2
	v_add_u32_e32 v3, v5, v3
	v_cmp_ne_u32_e32 vcc, v4, v3
	s_and_saveexec_b64 s[2:3], vcc
	s_xor_b64 s[10:11], exec, s[2:3]
	s_cbranch_execz .LBB0_269
	s_waitcnt lgkmcnt(0)
	v_mov_b32_e32 v1, 0
	global_load_dword v3, v1, s[98:99] sc1
	s_waitcnt vmcnt(0)
	v_cmp_eq_u32_e32 vcc, v3, v2
	s_and_saveexec_b64 s[12:13], vcc
	s_cbranch_execz .LBB0_268
	s_mov_b32 s2, 1
	s_mov_b64 s[14:15], 0
	s_branch .LBB0_259

; __device__ __forceinline__ unsigned xb_ld(unsigned* p)              { return __hip_atomic_load(p, __ATOMIC_RELAXED, __HIP_MEMORY_SCOPE_AGENT); }
; #define XB_SPIN(cond, bar) do { unsigned _sp = 0; while (cond) { __builtin_amdgcn_s_sleep(1); \
;     if ((++_sp & 255u) == 0u) { if (xb_ld(&(bar)[XB_TMO])) break; if (_sp > XB_SPIN_CAP) { atomicAdd(&(bar)[XB_TMO], 1u); break; } } } } while (0)
; __device__ __forceinline__ void xcd_barrier(const XcdBarrier& b) {
;     ...
;             XB_SPIN(xb_ld(&bar[XB_XGEN(b.x)]) == gen, bar);
.LBB0_261:
	global_load_dword v3, v1, s[98:99] sc1
	s_add_i32 s2, s2, 1
	s_mov_b64 s[34:35], -1
	s_waitcnt vmcnt(0)
	v_cmp_ne_u32_e32 vcc, v3, v2
	s_orn2_b64 s[18:19], vcc, exec
	s_branch .LBB0_258

; __device__ __forceinline__ unsigned xb_ld(unsigned* p)              { return __hip_atomic_load(p, __ATOMIC_RELAXED, __HIP_MEMORY_SCOPE_AGENT); }
; __device__ __forceinline__ unsigned xb_add(unsigned* p, unsigned v) { return __hip_atomic_fetch_add(p, v, __ATOMIC_RELAXED, __HIP_MEMORY_SCOPE_AGENT); }
; #define XB_SPIN(cond, bar) do { unsigned _sp = 0; while (cond) { __builtin_amdgcn_s_sleep(1); \
;     if ((++_sp & 255u) == 0u) { if (xb_ld(&(bar)[XB_TMO])) break; if (_sp > XB_SPIN_CAP) { atomicAdd(&(bar)[XB_TMO], 1u); break; } } } } while (0)
; __device__ __forceinline__ void xcd_barrier(const XcdBarrier& b) {
;     ...
;         if (nloc == 0u) { xcd_barrier_complete(bar, b.x, nloc, nx); b.st[0] = nloc; b.st[1] = nx; }
;         const unsigned old = xb_add(&bar[XB_XSUB(b.x)], 1u);
;         const unsigned gen = old / nloc;
;         if (old + 1u == (gen + 1u) * nloc) {
;             __builtin_amdgcn_fence(__ATOMIC_RELEASE, "agent");
;             asm volatile("s_waitcnt vmcnt(0)" ::: "memory");
;             const unsigned og = xb_add(&bar[XB_TOP], 1u);
;             const unsigned tg = og / nx;
;             if (og + 1u == (tg + 1u) * nx) xb_add(&bar[XB_TOPGEN], 1u);
;             else XB_SPIN(xb_ld(&bar[XB_TOPGEN]) == tg, bar);
;             __builtin_amdgcn_fence(__ATOMIC_ACQUIRE, "agent");
;             xb_add(&bar[XB_XGEN(b.x)], 1u);
;             asm volatile("s_waitcnt vmcnt(0)" ::: "memory");
;         } else {
;             XB_SPIN(xb_ld(&bar[XB_XGEN(b.x)]) == gen, bar);
.LBB0_1591:
	s_or_b64 exec, exec, s[8:9]
	v_cvt_f32_u32_e32 v4, v2
	s_waitcnt vmcnt(0)
	v_readfirstlane_b32 s6, v3
	s_add_u32 s4, s4, 0x2400
	s_addc_u32 s5, s5, 0
	s_add_u32 s98, s50, 0x7500
	s_addc_u32 s99, s51, 0
	v_rcp_iflag_f32_e32 v4, v4
	v_add_u32_e32 v5, s6, v1
	v_mul_f32_e32 v3, 0x4f7ffffe, v4
	v_cvt_u32_f32_e32 v3, v3
	v_sub_u32_e32 v4, 0, v2
	v_mul_lo_u32 v1, v4, v3
	v_mul_hi_u32 v1, v3, v1
	v_add_u32_e32 v1, v3, v1
	v_mul_hi_u32 v1, v5, v1
	v_mul_lo_u32 v3, v1, v2
	v_sub_u32_e32 v3, v5, v3
	v_add_u32_e32 v4, 1, v1
	v_cmp_ge_u32_e32 vcc, v3, v2
	s_nop 1
	v_cndmask_b32_e32 v1, v1, v4, vcc
	v_sub_u32_e32 v4, v3, v2
	v_cndmask_b32_e32 v3, v3, v4, vcc
	v_add_u32_e32 v4, 1, v1
	v_cmp_ge_u32_e32 vcc, v3, v2
	v_add_u32_e32 v3, 1, v5
	s_nop 0
	v_cndmask_b32_e32 v1, v1, v4, vcc
	v_mul_lo_u32 v4, v2, v1
	v_add_u32_e32 v2, v4, v2
	v_cmp_ne_u32_e32 vcc, v3, v2
	s_and_saveexec_b64 s[6:7], vcc
	s_xor_b64 s[6:7], exec, s[6:7]
	s_cbranch_execz .LBB0_1605
	s_waitcnt lgkmcnt(0)
	v_mov_b32_e32 v0, 0
	global_load_dword v2, v0, s[98:99] sc1
	s_waitcnt vmcnt(0)
	v_cmp_eq_u32_e32 vcc, v2, v1
	s_and_saveexec_b64 s[8:9], vcc
	s_cbranch_execz .LBB0_1604
	s_mov_b32 s20, 1
	s_mov_b64 s[10:11], 0
	s_branch .LBB0_1595

; __device__ __forceinline__ unsigned xb_ld(unsigned* p)              { return __hip_atomic_load(p, __ATOMIC_RELAXED, __HIP_MEMORY_SCOPE_AGENT); }
; #define XB_SPIN(cond, bar) do { unsigned _sp = 0; while (cond) { __builtin_amdgcn_s_sleep(1); \
;     if ((++_sp & 255u) == 0u) { if (xb_ld(&(bar)[XB_TMO])) break; if (_sp > XB_SPIN_CAP) { atomicAdd(&(bar)[XB_TMO], 1u); break; } } } } while (0)
; __device__ __forceinline__ void xcd_barrier(const XcdBarrier& b) {
;     ...
;             XB_SPIN(xb_ld(&bar[XB_XGEN(b.x)]) == gen, bar);
.LBB0_1597:
	global_load_dword v2, v0, s[98:99] sc1
	s_add_i32 s20, s20, 1
	s_mov_b64 s[16:17], -1
	s_waitcnt vmcnt(0)
	v_cmp_ne_u32_e32 vcc, v2, v1
	s_orn2_b64 s[14:15], vcc, exec
	s_branch .LBB0_1594
